# grid barrier: L1 invalidate issued at arrival by wave 1 with exec forced on (fixes k14 skipping it when exec=0), wait states kept
# baseline (speedup 1.0000x reference)
.LBB0_190:
	s_or_b64 exec, exec, s[4:5]
	v_readlane_b32 s4, v254, 16
	v_readlane_b32 s5, v254, 17
	s_waitcnt vmcnt(0)
	s_nop 0
	s_nop 2
	global_atomic_add v209, v231, s[4:5]
	s_waitcnt vmcnt(0)

.LBB0_204:
	s_waitcnt vmcnt(0)
	s_waitcnt vmcnt(0)
	s_barrier
	v_readlane_b32 s2, v254, 9
	s_nop 0
	s_cmp_lg_u32 s2, 64
	s_cbranch_scc1 .Lbinv_0
	s_mov_b64 s[2:3], exec
	s_mov_b64 exec, -1
	buffer_inv sc1
	s_waitcnt vmcnt(0)
	s_mov_b64 exec, s[2:3]

.LBB0_280:
	s_waitcnt vmcnt(0)
	s_waitcnt vmcnt(0) lgkmcnt(0)
	s_barrier
	v_readlane_b32 s4, v254, 9
	s_nop 0
	s_cmp_lg_u32 s4, 64
	s_cbranch_scc1 .Lbinv_1
	s_mov_b64 s[4:5], exec
	s_mov_b64 exec, -1
	buffer_inv sc1
	s_waitcnt vmcnt(0)
	s_mov_b64 exec, s[4:5]

.LBB0_327:
	s_or_b64 exec, exec, s[6:7]
	v_readlane_b32 s6, v254, 16
	v_readlane_b32 s7, v254, 17
	s_waitcnt vmcnt(0)
	s_nop 0
	s_nop 2
	global_atomic_add v209, v231, s[6:7]
	s_waitcnt vmcnt(0)

.LBB0_516:
	s_or_b64 exec, exec, s[8:9]
	v_readlane_b32 s2, v254, 16
	v_readlane_b32 s3, v254, 17
	s_waitcnt vmcnt(0)
	s_nop 0
	s_nop 2
	global_atomic_add v209, v231, s[2:3]
	s_waitcnt vmcnt(0)

.LBB0_537:
	s_waitcnt vmcnt(0)
	s_waitcnt vmcnt(0) lgkmcnt(0)
	s_barrier
	v_readlane_b32 s2, v254, 9
	s_nop 0
	s_cmp_lg_u32 s2, 64
	s_cbranch_scc1 .Lbinv_4
	s_mov_b64 s[2:3], exec
	s_mov_b64 exec, -1
	buffer_inv sc1
	s_waitcnt vmcnt(0)
	s_mov_b64 exec, s[2:3]

.LBB0_1296:
	s_waitcnt vmcnt(0)
	s_barrier
	v_readlane_b32 s2, v254, 9
	s_nop 0
	s_cmp_lg_u32 s2, 64
	s_cbranch_scc1 .Lbinv_10
	s_mov_b64 s[2:3], exec
	s_mov_b64 exec, -1
	buffer_inv sc1
	s_waitcnt vmcnt(0)
	s_mov_b64 exec, s[2:3]
